# gla_c: state tensor KVS stored fragment-major by the scan phase so the MFMA operand loads are 1 KB contiguous per wave; the 36 fragment loads of a direction issued up front with counted vmcnt (plus NA
# speedup vs baseline: 1.0054x; 1.0054x over previous
.LBB0_993:
	v_and_b32_e32 v4, 0x7e, v147
	s_mov_b32 s12, 0x40000
	v_ashrrev_i32_e32 v150, 14, v146
	v_cmp_gt_u32_e32 vcc, s12, v146
	v_lshlrev_b32_e32 v2, 1, v4
	v_lshlrev_b32_e32 v4, 2, v4
	v_mov_b32_e32 v5, v97
	v_mul_i32_i24_e32 v10, 36, v150
	v_and_b32_e32 v0, 0x7f80, v147
	v_lshl_add_u64 v[6:7], s[8:9], 0, v[4:5]
	v_cndmask_b32_e64 v4, 3, 0, vcc
	v_lshlrev_b32_e32 v96, 1, v0
	v_or_b32_e32 v4, v4, v10
	v_lshl_add_u64 v[0:1], s[4:5], 0, v[96:97]
	v_mov_b32_e32 v3, v97
	v_ashrrev_i32_e32 v5, 31, v4
	v_lshl_add_u64 v[0:1], v[0:1], 0, v[2:3]
	v_lshlrev_b64 v[142:143], 16, v[4:5]
	v_lshlrev_b64 v[4:5], 9, v[4:5]
	v_lshl_add_u64 v[8:9], v[0:1], 0, v[142:143]
	v_lshl_add_u64 v[4:5], v[6:7], 0, v[4:5]
	global_load_dword v151, v[8:9], off
	global_load_dwordx2 v[144:145], v[4:5], off
	v_cndmask_b32_e64 v4, 2, 1, vcc
	v_or_b32_e32 v4, v4, v10
	v_ashrrev_i32_e32 v5, 31, v4
	v_lshlrev_b64 v[138:139], 16, v[4:5]
	v_lshlrev_b64 v[4:5], 9, v[4:5]
	v_lshl_add_u64 v[8:9], v[0:1], 0, v[138:139]
	v_lshl_add_u64 v[4:5], v[6:7], 0, v[4:5]
	global_load_dword v152, v[8:9], off
	global_load_dwordx2 v[140:141], v[4:5], off
	v_cndmask_b32_e64 v4, 1, 2, vcc
	v_or_b32_e32 v4, v4, v10
	v_ashrrev_i32_e32 v5, 31, v4
	v_lshlrev_b64 v[134:135], 16, v[4:5]
	v_lshlrev_b64 v[4:5], 9, v[4:5]
	v_lshl_add_u64 v[8:9], v[0:1], 0, v[134:135]
	v_lshl_add_u64 v[4:5], v[6:7], 0, v[4:5]
	global_load_dword v153, v[8:9], off
	global_load_dwordx2 v[136:137], v[4:5], off
	v_cndmask_b32_e64 v4, 0, 3, vcc
	v_or_b32_e32 v4, v4, v10
	v_ashrrev_i32_e32 v5, 31, v4
	v_lshlrev_b64 v[130:131], 16, v[4:5]
	v_lshlrev_b64 v[4:5], 9, v[4:5]
	v_lshl_add_u64 v[8:9], v[0:1], 0, v[130:131]
	v_lshl_add_u64 v[4:5], v[6:7], 0, v[4:5]
	global_load_dword v154, v[8:9], off
	global_load_dwordx2 v[132:133], v[4:5], off
	v_cndmask_b32_e64 v4, 35, 4, vcc
	v_mad_i32_i24 v4, v150, 36, v4
	v_ashrrev_i32_e32 v5, 31, v4
	v_lshlrev_b64 v[126:127], 16, v[4:5]
	v_lshlrev_b64 v[4:5], 9, v[4:5]
	v_lshl_add_u64 v[8:9], v[0:1], 0, v[126:127]
	v_lshl_add_u64 v[4:5], v[6:7], 0, v[4:5]
	global_load_dword v155, v[8:9], off
	global_load_dwordx2 v[128:129], v[4:5], off
	v_cndmask_b32_e64 v4, 34, 5, vcc
	v_mad_i32_i24 v4, v150, 36, v4
	v_ashrrev_i32_e32 v5, 31, v4
	v_lshlrev_b64 v[122:123], 16, v[4:5]
	v_lshlrev_b64 v[4:5], 9, v[4:5]
	v_lshl_add_u64 v[8:9], v[0:1], 0, v[122:123]
	v_lshl_add_u64 v[4:5], v[6:7], 0, v[4:5]
	global_load_dword v156, v[8:9], off
	global_load_dwordx2 v[124:125], v[4:5], off
	v_cndmask_b32_e64 v4, 33, 6, vcc
	v_mad_i32_i24 v4, v150, 36, v4
	v_ashrrev_i32_e32 v5, 31, v4
	v_lshlrev_b64 v[118:119], 16, v[4:5]
	v_lshlrev_b64 v[4:5], 9, v[4:5]
	v_lshl_add_u64 v[8:9], v[0:1], 0, v[118:119]
	v_lshl_add_u64 v[4:5], v[6:7], 0, v[4:5]
	global_load_dword v157, v[8:9], off
	global_load_dwordx2 v[120:121], v[4:5], off
	v_cndmask_b32_e64 v4, 32, 7, vcc
	v_mad_i32_i24 v4, v150, 36, v4
	v_ashrrev_i32_e32 v5, 31, v4
	v_lshlrev_b64 v[114:115], 16, v[4:5]
	v_lshlrev_b64 v[4:5], 9, v[4:5]
	v_lshl_add_u64 v[8:9], v[0:1], 0, v[114:115]
	v_lshl_add_u64 v[4:5], v[6:7], 0, v[4:5]
	global_load_dword v158, v[8:9], off
	global_load_dwordx2 v[116:117], v[4:5], off
	v_cndmask_b32_e64 v4, 31, 8, vcc
	v_mad_i32_i24 v4, v150, 36, v4
	v_ashrrev_i32_e32 v5, 31, v4
	v_lshlrev_b64 v[110:111], 16, v[4:5]
	v_lshlrev_b64 v[4:5], 9, v[4:5]
	v_lshl_add_u64 v[8:9], v[0:1], 0, v[110:111]
	v_lshl_add_u64 v[4:5], v[6:7], 0, v[4:5]
	global_load_dword v159, v[8:9], off
	global_load_dwordx2 v[112:113], v[4:5], off
	v_cndmask_b32_e64 v4, 30, 9, vcc
	v_mad_i32_i24 v4, v150, 36, v4
	v_ashrrev_i32_e32 v5, 31, v4
	v_lshlrev_b64 v[106:107], 16, v[4:5]
	v_lshlrev_b64 v[4:5], 9, v[4:5]
	v_lshl_add_u64 v[8:9], v[0:1], 0, v[106:107]
	v_lshl_add_u64 v[4:5], v[6:7], 0, v[4:5]
	global_load_dword v160, v[8:9], off
	global_load_dwordx2 v[108:109], v[4:5], off
	v_cndmask_b32_e64 v4, 29, 10, vcc
	v_mad_i32_i24 v4, v150, 36, v4
	v_ashrrev_i32_e32 v5, 31, v4
	v_lshlrev_b64 v[102:103], 16, v[4:5]
	v_lshlrev_b64 v[4:5], 9, v[4:5]
	v_lshl_add_u64 v[8:9], v[0:1], 0, v[102:103]
	v_lshl_add_u64 v[4:5], v[6:7], 0, v[4:5]
	global_load_dword v161, v[8:9], off
	global_load_dwordx2 v[104:105], v[4:5], off
	v_cndmask_b32_e64 v4, 28, 11, vcc
	v_mad_i32_i24 v4, v150, 36, v4
	v_ashrrev_i32_e32 v5, 31, v4
	v_lshlrev_b64 v[98:99], 16, v[4:5]
	v_lshlrev_b64 v[4:5], 9, v[4:5]
	v_lshl_add_u64 v[8:9], v[0:1], 0, v[98:99]
	v_lshl_add_u64 v[4:5], v[6:7], 0, v[4:5]
	global_load_dword v162, v[8:9], off
	global_load_dwordx2 v[100:101], v[4:5], off
	v_cndmask_b32_e64 v4, 27, 12, vcc
	v_mad_i32_i24 v4, v150, 36, v4
	v_ashrrev_i32_e32 v5, 31, v4
	v_lshlrev_b64 v[92:93], 16, v[4:5]
	v_lshlrev_b64 v[4:5], 9, v[4:5]
	v_lshl_add_u64 v[8:9], v[0:1], 0, v[92:93]
	v_lshl_add_u64 v[4:5], v[6:7], 0, v[4:5]
	global_load_dword v163, v[8:9], off
	global_load_dwordx2 v[94:95], v[4:5], off
	v_cndmask_b32_e64 v4, 26, 13, vcc
	v_mad_i32_i24 v4, v150, 36, v4
	v_ashrrev_i32_e32 v5, 31, v4
	v_lshlrev_b64 v[88:89], 16, v[4:5]
	v_lshlrev_b64 v[4:5], 9, v[4:5]
	v_lshl_add_u64 v[8:9], v[0:1], 0, v[88:89]
	v_lshl_add_u64 v[4:5], v[6:7], 0, v[4:5]
	global_load_dword v164, v[8:9], off
	global_load_dwordx2 v[90:91], v[4:5], off
	v_cndmask_b32_e64 v4, 25, 14, vcc
	v_mad_i32_i24 v4, v150, 36, v4
	v_ashrrev_i32_e32 v5, 31, v4
	v_lshlrev_b64 v[84:85], 16, v[4:5]
	v_lshlrev_b64 v[4:5], 9, v[4:5]
	v_lshl_add_u64 v[8:9], v[0:1], 0, v[84:85]
	v_lshl_add_u64 v[4:5], v[6:7], 0, v[4:5]
	global_load_dword v165, v[8:9], off
	global_load_dwordx2 v[86:87], v[4:5], off
	v_cndmask_b32_e64 v4, 24, 15, vcc
	v_mad_i32_i24 v4, v150, 36, v4
	v_ashrrev_i32_e32 v5, 31, v4
	v_lshlrev_b64 v[80:81], 16, v[4:5]
	v_lshlrev_b64 v[4:5], 9, v[4:5]
	v_lshl_add_u64 v[8:9], v[0:1], 0, v[80:81]
	v_lshl_add_u64 v[4:5], v[6:7], 0, v[4:5]
	global_load_dword v166, v[8:9], off
	global_load_dwordx2 v[82:83], v[4:5], off
	v_cndmask_b32_e64 v4, 23, 16, vcc
	v_mad_i32_i24 v4, v150, 36, v4
	v_ashrrev_i32_e32 v5, 31, v4
	v_lshlrev_b64 v[76:77], 16, v[4:5]
	v_lshlrev_b64 v[4:5], 9, v[4:5]
	v_lshl_add_u64 v[8:9], v[0:1], 0, v[76:77]
	v_lshl_add_u64 v[4:5], v[6:7], 0, v[4:5]
	global_load_dword v167, v[8:9], off
	global_load_dwordx2 v[78:79], v[4:5], off
	v_cndmask_b32_e64 v4, 22, 17, vcc
	v_mad_i32_i24 v4, v150, 36, v4
	v_ashrrev_i32_e32 v5, 31, v4
	v_lshlrev_b64 v[72:73], 16, v[4:5]
	v_lshlrev_b64 v[4:5], 9, v[4:5]
	v_lshl_add_u64 v[8:9], v[0:1], 0, v[72:73]
	v_lshl_add_u64 v[4:5], v[6:7], 0, v[4:5]
	global_load_dword v168, v[8:9], off
	global_load_dwordx2 v[74:75], v[4:5], off
	v_cndmask_b32_e64 v4, 21, 18, vcc
	v_mad_i32_i24 v4, v150, 36, v4
	v_ashrrev_i32_e32 v5, 31, v4
	v_lshlrev_b64 v[68:69], 16, v[4:5]
	v_lshlrev_b64 v[4:5], 9, v[4:5]
	v_lshl_add_u64 v[8:9], v[0:1], 0, v[68:69]
	v_lshl_add_u64 v[4:5], v[6:7], 0, v[4:5]
	global_load_dword v169, v[8:9], off
	global_load_dwordx2 v[70:71], v[4:5], off
	v_cndmask_b32_e64 v4, 20, 19, vcc
	v_mad_i32_i24 v4, v150, 36, v4
	v_ashrrev_i32_e32 v5, 31, v4
	v_lshlrev_b64 v[64:65], 16, v[4:5]
	v_lshlrev_b64 v[4:5], 9, v[4:5]
	v_lshl_add_u64 v[8:9], v[0:1], 0, v[64:65]
	v_lshl_add_u64 v[4:5], v[6:7], 0, v[4:5]
	global_load_dword v170, v[8:9], off
	global_load_dwordx2 v[66:67], v[4:5], off
	v_cndmask_b32_e64 v4, 19, 20, vcc
	v_mad_i32_i24 v4, v150, 36, v4
	v_ashrrev_i32_e32 v5, 31, v4
	v_lshlrev_b64 v[60:61], 16, v[4:5]
	v_lshlrev_b64 v[4:5], 9, v[4:5]
	v_lshl_add_u64 v[8:9], v[0:1], 0, v[60:61]
	v_lshl_add_u64 v[4:5], v[6:7], 0, v[4:5]
	global_load_dword v171, v[8:9], off
	global_load_dwordx2 v[62:63], v[4:5], off
	v_cndmask_b32_e64 v4, 18, 21, vcc
	v_mad_i32_i24 v4, v150, 36, v4
	v_ashrrev_i32_e32 v5, 31, v4
	v_lshlrev_b64 v[56:57], 16, v[4:5]
	v_lshlrev_b64 v[4:5], 9, v[4:5]
	v_lshl_add_u64 v[8:9], v[0:1], 0, v[56:57]
	v_lshl_add_u64 v[4:5], v[6:7], 0, v[4:5]
	global_load_dword v172, v[8:9], off
	global_load_dwordx2 v[58:59], v[4:5], off
	v_cndmask_b32_e64 v4, 17, 22, vcc
	v_mad_i32_i24 v4, v150, 36, v4
	v_ashrrev_i32_e32 v5, 31, v4
	v_lshlrev_b64 v[52:53], 16, v[4:5]
	v_lshlrev_b64 v[4:5], 9, v[4:5]
	v_lshl_add_u64 v[8:9], v[0:1], 0, v[52:53]
	v_lshl_add_u64 v[4:5], v[6:7], 0, v[4:5]
	global_load_dword v173, v[8:9], off
	global_load_dwordx2 v[54:55], v[4:5], off
	v_cndmask_b32_e64 v4, 16, 23, vcc
	v_mad_i32_i24 v4, v150, 36, v4
	v_ashrrev_i32_e32 v5, 31, v4
	v_lshlrev_b64 v[48:49], 16, v[4:5]
	v_lshlrev_b64 v[4:5], 9, v[4:5]
	v_lshl_add_u64 v[8:9], v[0:1], 0, v[48:49]
	v_lshl_add_u64 v[4:5], v[6:7], 0, v[4:5]
	global_load_dword v174, v[8:9], off
	global_load_dwordx2 v[50:51], v[4:5], off
	v_cndmask_b32_e64 v4, 15, 24, vcc
	v_mad_i32_i24 v4, v150, 36, v4
	v_ashrrev_i32_e32 v5, 31, v4
	v_lshlrev_b64 v[44:45], 16, v[4:5]
	v_lshlrev_b64 v[4:5], 9, v[4:5]
	v_lshl_add_u64 v[8:9], v[0:1], 0, v[44:45]
	v_lshl_add_u64 v[4:5], v[6:7], 0, v[4:5]
	global_load_dword v175, v[8:9], off
	global_load_dwordx2 v[46:47], v[4:5], off
	v_cndmask_b32_e64 v4, 14, 25, vcc
	v_mad_i32_i24 v4, v150, 36, v4
	v_ashrrev_i32_e32 v5, 31, v4
	v_lshlrev_b64 v[40:41], 16, v[4:5]
	v_lshlrev_b64 v[4:5], 9, v[4:5]
	v_lshl_add_u64 v[8:9], v[0:1], 0, v[40:41]
	v_lshl_add_u64 v[4:5], v[6:7], 0, v[4:5]
	global_load_dword v176, v[8:9], off
	global_load_dwordx2 v[42:43], v[4:5], off
	v_cndmask_b32_e64 v4, 13, 26, vcc
	v_mad_i32_i24 v4, v150, 36, v4
	v_ashrrev_i32_e32 v5, 31, v4
	v_lshlrev_b64 v[36:37], 16, v[4:5]
	v_lshlrev_b64 v[4:5], 9, v[4:5]
	v_lshl_add_u64 v[8:9], v[0:1], 0, v[36:37]
	v_lshl_add_u64 v[4:5], v[6:7], 0, v[4:5]
	global_load_dword v177, v[8:9], off
	global_load_dwordx2 v[38:39], v[4:5], off
	v_cndmask_b32_e64 v4, 12, 27, vcc
	v_mad_i32_i24 v4, v150, 36, v4
	v_ashrrev_i32_e32 v5, 31, v4
	v_lshlrev_b64 v[32:33], 16, v[4:5]
	v_lshlrev_b64 v[4:5], 9, v[4:5]
	v_lshl_add_u64 v[8:9], v[0:1], 0, v[32:33]
	v_lshl_add_u64 v[4:5], v[6:7], 0, v[4:5]
	global_load_dword v178, v[8:9], off
	global_load_dwordx2 v[34:35], v[4:5], off
	v_cndmask_b32_e64 v4, 11, 28, vcc
	v_mad_i32_i24 v4, v150, 36, v4
	v_ashrrev_i32_e32 v5, 31, v4
	v_lshlrev_b64 v[28:29], 16, v[4:5]
	v_lshlrev_b64 v[4:5], 9, v[4:5]
	v_lshl_add_u64 v[8:9], v[0:1], 0, v[28:29]
	v_lshl_add_u64 v[4:5], v[6:7], 0, v[4:5]
	global_load_dword v179, v[8:9], off
	global_load_dwordx2 v[30:31], v[4:5], off
	v_cndmask_b32_e64 v4, 10, 29, vcc
	v_mad_i32_i24 v4, v150, 36, v4
	v_ashrrev_i32_e32 v5, 31, v4
	v_lshlrev_b64 v[24:25], 16, v[4:5]
	v_lshlrev_b64 v[4:5], 9, v[4:5]
	v_lshl_add_u64 v[8:9], v[0:1], 0, v[24:25]
	v_lshl_add_u64 v[4:5], v[6:7], 0, v[4:5]
	global_load_dword v180, v[8:9], off
	global_load_dwordx2 v[26:27], v[4:5], off
	v_cndmask_b32_e64 v4, 9, 30, vcc
	v_mad_i32_i24 v4, v150, 36, v4
	v_ashrrev_i32_e32 v5, 31, v4
	v_lshlrev_b64 v[20:21], 16, v[4:5]
	v_lshlrev_b64 v[4:5], 9, v[4:5]
	v_lshl_add_u64 v[8:9], v[0:1], 0, v[20:21]
	v_lshl_add_u64 v[4:5], v[6:7], 0, v[4:5]
	global_load_dword v181, v[8:9], off
	global_load_dwordx2 v[22:23], v[4:5], off
	v_cndmask_b32_e64 v4, 8, 31, vcc
	v_mad_i32_i24 v4, v150, 36, v4
	v_ashrrev_i32_e32 v5, 31, v4
	v_lshlrev_b64 v[16:17], 16, v[4:5]
	v_lshlrev_b64 v[4:5], 9, v[4:5]
	v_lshl_add_u64 v[8:9], v[0:1], 0, v[16:17]
	v_lshl_add_u64 v[4:5], v[6:7], 0, v[4:5]
	global_load_dword v182, v[8:9], off
	global_load_dwordx2 v[18:19], v[4:5], off
	v_cndmask_b32_e64 v4, 7, 32, vcc
	v_mad_i32_i24 v4, v150, 36, v4
	v_ashrrev_i32_e32 v5, 31, v4
	v_lshlrev_b64 v[12:13], 16, v[4:5]
	v_lshlrev_b64 v[4:5], 9, v[4:5]
	v_lshl_add_u64 v[8:9], v[0:1], 0, v[12:13]
	v_lshl_add_u64 v[4:5], v[6:7], 0, v[4:5]
	global_load_dword v183, v[8:9], off
	global_load_dwordx2 v[14:15], v[4:5], off
	v_cndmask_b32_e64 v4, 6, 33, vcc
	v_mad_i32_i24 v4, v150, 36, v4
	v_ashrrev_i32_e32 v5, 31, v4
	v_lshlrev_b64 v[8:9], 16, v[4:5]
	v_lshlrev_b64 v[4:5], 9, v[4:5]
	v_lshl_add_u64 v[10:11], v[0:1], 0, v[8:9]
	v_lshl_add_u64 v[4:5], v[6:7], 0, v[4:5]
	global_load_dword v184, v[10:11], off
	v_add_u32_e32 v146, s97, v146
	global_load_dwordx2 v[10:11], v[4:5], off
	v_cndmask_b32_e64 v4, 5, 34, vcc
	v_mad_i32_i24 v148, v150, 36, v4
	v_ashrrev_i32_e32 v149, 31, v148
	v_lshlrev_b64 v[4:5], 16, v[148:149]
	v_lshl_add_u64 v[0:1], v[0:1], 0, v[4:5]
	global_load_dword v185, v[0:1], off
	v_lshlrev_b64 v[0:1], 9, v[148:149]
	v_and_b32_e32 v2, 0x1e, v147
	v_lshlrev_b32_e32 v2, 1, v2
	v_bfe_u32 v3, v147, 5, 2
	v_lshl_or_b32 v2, v3, 10, v2
	v_bfe_u32 v3, v147, 7, 4
	v_lshl_or_b32 v2, v3, 6, v2
	v_bfe_u32 v3, v147, 11, 4
	v_lshl_or_b32 v2, v3, 12, v2
	v_mov_b32_e32 v3, v97
	v_lshl_add_u64 v[2:3], s[6:7], 0, v[2:3]
	v_lshl_add_u64 v[0:1], v[6:7], 0, v[0:1]
	v_lshl_add_u64 v[142:143], v[2:3], 0, v[142:143]
	s_waitcnt vmcnt(0)
	v_lshlrev_b32_e32 v96, 16, v151
	global_load_dwordx2 v[6:7], v[0:1], off
	v_fmac_f32_e32 v96, 0, v144
	global_store_dword v[142:143], v97, off
	v_and_b32_e32 v142, 0xffff0000, v151
	v_fmac_f32_e32 v142, 0, v145
	v_bfe_u32 v143, v96, 16, 1
	v_add3_u32 v143, v96, v143, s51
	v_bfe_u32 v144, v142, 16, 1
	v_lshrrev_b32_e32 v143, 16, v143
	v_add3_u32 v144, v142, v144, s51
	v_and_or_b32 v143, v144, s48, v143
	v_lshl_add_u64 v[138:139], v[2:3], 0, v[138:139]
	global_store_dword v[138:139], v143, off
	v_lshlrev_b32_e32 v138, 16, v152
	v_fmac_f32_e32 v138, v96, v140
	v_and_b32_e32 v96, 0xffff0000, v152
	v_fmac_f32_e32 v96, v142, v141
	v_bfe_u32 v139, v138, 16, 1
	v_add3_u32 v139, v138, v139, s51
	v_bfe_u32 v140, v96, 16, 1
	v_lshrrev_b32_e32 v139, 16, v139
	v_add3_u32 v140, v96, v140, s51
	v_and_or_b32 v139, v140, s48, v139
	v_lshl_add_u64 v[134:135], v[2:3], 0, v[134:135]
	global_store_dword v[134:135], v139, off
	v_lshlrev_b32_e32 v134, 16, v153
	v_fmac_f32_e32 v134, v138, v136
	v_and_b32_e32 v135, 0xffff0000, v153
	v_fmac_f32_e32 v135, v96, v137
	v_bfe_u32 v96, v134, 16, 1
	v_add3_u32 v96, v134, v96, s51
	v_bfe_u32 v136, v135, 16, 1
	v_lshrrev_b32_e32 v96, 16, v96
	v_add3_u32 v136, v135, v136, s51
	v_and_or_b32 v96, v136, s48, v96
	v_lshl_add_u64 v[130:131], v[2:3], 0, v[130:131]
	global_store_dword v[130:131], v96, off
	v_lshlrev_b32_e32 v96, 16, v154
	s_waitcnt vmcnt(62)
	v_fmac_f32_e32 v96, v134, v132
	v_and_b32_e32 v130, 0xffff0000, v154
	v_fmac_f32_e32 v130, v135, v133
	v_bfe_u32 v131, v96, 16, 1
	v_add3_u32 v131, v96, v131, s51
	v_bfe_u32 v132, v130, 16, 1
	v_lshrrev_b32_e32 v131, 16, v131
	v_add3_u32 v132, v130, v132, s51
	v_and_or_b32 v131, v132, s48, v131
	v_lshl_add_u64 v[126:127], v[2:3], 0, v[126:127]
	global_store_dword v[126:127], v131, off
	v_lshlrev_b32_e32 v126, 16, v155
	v_fmac_f32_e32 v126, v96, v128
	v_and_b32_e32 v96, 0xffff0000, v155
	v_fmac_f32_e32 v96, v130, v129
	v_bfe_u32 v127, v126, 16, 1
	v_add3_u32 v127, v126, v127, s51
	v_bfe_u32 v128, v96, 16, 1
	v_lshrrev_b32_e32 v127, 16, v127
	v_add3_u32 v128, v96, v128, s51
	v_and_or_b32 v127, v128, s48, v127
	v_lshl_add_u64 v[122:123], v[2:3], 0, v[122:123]
	global_store_dword v[122:123], v127, off
	v_lshlrev_b32_e32 v122, 16, v156
	v_fmac_f32_e32 v122, v126, v124
	v_and_b32_e32 v123, 0xffff0000, v156
	v_fmac_f32_e32 v123, v96, v125
	v_bfe_u32 v96, v122, 16, 1
	v_add3_u32 v96, v122, v96, s51
	v_bfe_u32 v124, v123, 16, 1
	v_lshrrev_b32_e32 v96, 16, v96
	v_add3_u32 v124, v123, v124, s51
	v_and_or_b32 v96, v124, s48, v96
	v_lshl_add_u64 v[118:119], v[2:3], 0, v[118:119]
	global_store_dword v[118:119], v96, off
	s_waitcnt vmcnt(62)
	v_lshlrev_b32_e32 v96, 16, v157
	v_fmac_f32_e32 v96, v122, v120
	v_and_b32_e32 v118, 0xffff0000, v157
	v_fmac_f32_e32 v118, v123, v121
	v_bfe_u32 v119, v96, 16, 1
	v_add3_u32 v119, v96, v119, s51
	v_bfe_u32 v120, v118, 16, 1
	v_lshrrev_b32_e32 v119, 16, v119
	v_add3_u32 v120, v118, v120, s51
	v_and_or_b32 v119, v120, s48, v119
	v_lshl_add_u64 v[114:115], v[2:3], 0, v[114:115]
	global_store_dword v[114:115], v119, off
	v_lshlrev_b32_e32 v114, 16, v158
	s_waitcnt vmcnt(62)
	v_fmac_f32_e32 v114, v96, v116
	v_and_b32_e32 v96, 0xffff0000, v158
	v_fmac_f32_e32 v96, v118, v117
	v_bfe_u32 v115, v114, 16, 1
	v_add3_u32 v115, v114, v115, s51
	v_bfe_u32 v116, v96, 16, 1
	v_lshrrev_b32_e32 v115, 16, v115
	v_add3_u32 v116, v96, v116, s51
	v_and_or_b32 v115, v116, s48, v115
	v_lshl_add_u64 v[110:111], v[2:3], 0, v[110:111]
	global_store_dword v[110:111], v115, off
	s_waitcnt vmcnt(62)
	v_lshlrev_b32_e32 v110, 16, v159
	s_waitcnt vmcnt(61)
	v_fmac_f32_e32 v110, v114, v112
	v_and_b32_e32 v111, 0xffff0000, v159
	v_fmac_f32_e32 v111, v96, v113
	v_bfe_u32 v96, v110, 16, 1
	v_add3_u32 v96, v110, v96, s51
	v_bfe_u32 v112, v111, 16, 1
	v_lshrrev_b32_e32 v96, 16, v96
	v_add3_u32 v112, v111, v112, s51
	v_and_or_b32 v96, v112, s48, v96
	v_lshl_add_u64 v[106:107], v[2:3], 0, v[106:107]
	global_store_dword v[106:107], v96, off
	s_waitcnt vmcnt(61)
	v_lshlrev_b32_e32 v96, 16, v160
	s_waitcnt vmcnt(60)
	v_fmac_f32_e32 v96, v110, v108
	v_and_b32_e32 v106, 0xffff0000, v160
	v_fmac_f32_e32 v106, v111, v109
	v_bfe_u32 v107, v96, 16, 1
	v_add3_u32 v107, v96, v107, s51
	v_bfe_u32 v108, v106, 16, 1
	v_lshrrev_b32_e32 v107, 16, v107
	v_add3_u32 v108, v106, v108, s51
	v_and_or_b32 v107, v108, s48, v107
	v_lshl_add_u64 v[102:103], v[2:3], 0, v[102:103]
	global_store_dword v[102:103], v107, off
	s_waitcnt vmcnt(60)
	v_lshlrev_b32_e32 v102, 16, v161
	s_waitcnt vmcnt(59)
	v_fmac_f32_e32 v102, v96, v104
	v_and_b32_e32 v96, 0xffff0000, v161
	v_fmac_f32_e32 v96, v106, v105
	v_bfe_u32 v103, v102, 16, 1
	v_add3_u32 v103, v102, v103, s51
	v_bfe_u32 v104, v96, 16, 1
	v_lshrrev_b32_e32 v103, 16, v103
	v_add3_u32 v104, v96, v104, s51
	v_and_or_b32 v103, v104, s48, v103
	v_lshl_add_u64 v[98:99], v[2:3], 0, v[98:99]
	global_store_dword v[98:99], v103, off
	s_waitcnt vmcnt(59)
	v_lshlrev_b32_e32 v98, 16, v162
	s_waitcnt vmcnt(58)
	v_fmac_f32_e32 v98, v102, v100
	v_and_b32_e32 v99, 0xffff0000, v162
	v_fmac_f32_e32 v99, v96, v101
	v_bfe_u32 v96, v98, 16, 1
	v_add3_u32 v96, v98, v96, s51
	v_bfe_u32 v100, v99, 16, 1
	v_lshrrev_b32_e32 v96, 16, v96
	v_add3_u32 v100, v99, v100, s51
	v_and_or_b32 v96, v100, s48, v96
	v_lshl_add_u64 v[92:93], v[2:3], 0, v[92:93]
	global_store_dword v[92:93], v96, off
	s_waitcnt vmcnt(58)
	v_lshlrev_b32_e32 v92, 16, v163
	s_waitcnt vmcnt(57)
	v_fmac_f32_e32 v92, v98, v94
	v_and_b32_e32 v93, 0xffff0000, v163
	v_fmac_f32_e32 v93, v99, v95
	v_bfe_u32 v94, v92, 16, 1
	v_add3_u32 v94, v92, v94, s51
	v_bfe_u32 v95, v93, 16, 1
	v_lshrrev_b32_e32 v94, 16, v94
	v_add3_u32 v95, v93, v95, s51
	v_and_or_b32 v94, v95, s48, v94
	v_lshl_add_u64 v[88:89], v[2:3], 0, v[88:89]
	global_store_dword v[88:89], v94, off
	s_waitcnt vmcnt(57)
	v_lshlrev_b32_e32 v88, 16, v164
	s_waitcnt vmcnt(56)
	v_fmac_f32_e32 v88, v92, v90
	v_and_b32_e32 v89, 0xffff0000, v164
	v_fmac_f32_e32 v89, v93, v91
	v_bfe_u32 v90, v88, 16, 1
	v_add3_u32 v90, v88, v90, s51
	v_bfe_u32 v91, v89, 16, 1
	v_lshrrev_b32_e32 v90, 16, v90
	v_add3_u32 v91, v89, v91, s51
	v_and_or_b32 v90, v91, s48, v90
	v_lshl_add_u64 v[84:85], v[2:3], 0, v[84:85]
	global_store_dword v[84:85], v90, off
	s_waitcnt vmcnt(56)
	v_lshlrev_b32_e32 v84, 16, v165
	s_waitcnt vmcnt(55)
	v_fmac_f32_e32 v84, v88, v86
	v_and_b32_e32 v85, 0xffff0000, v165
	v_fmac_f32_e32 v85, v89, v87
	v_bfe_u32 v86, v84, 16, 1
	v_add3_u32 v86, v84, v86, s51
	v_bfe_u32 v87, v85, 16, 1
	v_lshrrev_b32_e32 v86, 16, v86
	v_add3_u32 v87, v85, v87, s51
	v_and_or_b32 v86, v87, s48, v86
	v_lshl_add_u64 v[80:81], v[2:3], 0, v[80:81]
	global_store_dword v[80:81], v86, off
	s_waitcnt vmcnt(55)
	v_lshlrev_b32_e32 v80, 16, v166
	s_waitcnt vmcnt(54)
	v_fmac_f32_e32 v80, v84, v82
	v_and_b32_e32 v81, 0xffff0000, v166
	v_fmac_f32_e32 v81, v85, v83
	v_bfe_u32 v82, v80, 16, 1
	v_add3_u32 v82, v80, v82, s51
	v_bfe_u32 v83, v81, 16, 1
	v_lshrrev_b32_e32 v82, 16, v82
	v_add3_u32 v83, v81, v83, s51
	v_and_or_b32 v82, v83, s48, v82
	v_lshl_add_u64 v[76:77], v[2:3], 0, v[76:77]
	global_store_dword v[76:77], v82, off
	s_waitcnt vmcnt(54)
	v_lshlrev_b32_e32 v76, 16, v167
	s_waitcnt vmcnt(53)
	v_fmac_f32_e32 v76, v80, v78
	v_and_b32_e32 v77, 0xffff0000, v167
	v_fmac_f32_e32 v77, v81, v79
	v_bfe_u32 v78, v76, 16, 1
	v_add3_u32 v78, v76, v78, s51
	v_bfe_u32 v79, v77, 16, 1
	v_lshrrev_b32_e32 v78, 16, v78
	v_add3_u32 v79, v77, v79, s51
	v_and_or_b32 v78, v79, s48, v78
	v_lshl_add_u64 v[72:73], v[2:3], 0, v[72:73]
	global_store_dword v[72:73], v78, off
	s_waitcnt vmcnt(53)
	v_lshlrev_b32_e32 v72, 16, v168
	s_waitcnt vmcnt(52)
	v_fmac_f32_e32 v72, v76, v74
	v_and_b32_e32 v73, 0xffff0000, v168
	v_fmac_f32_e32 v73, v77, v75
	v_bfe_u32 v74, v72, 16, 1
	v_add3_u32 v74, v72, v74, s51
	v_bfe_u32 v75, v73, 16, 1
	v_lshrrev_b32_e32 v74, 16, v74
	v_add3_u32 v75, v73, v75, s51
	v_and_or_b32 v74, v75, s48, v74
	v_lshl_add_u64 v[68:69], v[2:3], 0, v[68:69]
	global_store_dword v[68:69], v74, off
	s_waitcnt vmcnt(52)
	v_lshlrev_b32_e32 v68, 16, v169
	s_waitcnt vmcnt(51)
	v_fmac_f32_e32 v68, v72, v70
	v_and_b32_e32 v69, 0xffff0000, v169
	v_fmac_f32_e32 v69, v73, v71
	v_bfe_u32 v70, v68, 16, 1
	v_add3_u32 v70, v68, v70, s51
	v_bfe_u32 v71, v69, 16, 1
	v_lshrrev_b32_e32 v70, 16, v70
	v_add3_u32 v71, v69, v71, s51
	v_and_or_b32 v70, v71, s48, v70
	v_lshl_add_u64 v[64:65], v[2:3], 0, v[64:65]
	global_store_dword v[64:65], v70, off
	s_waitcnt vmcnt(51)
	v_lshlrev_b32_e32 v64, 16, v170
	s_waitcnt vmcnt(50)
	v_fmac_f32_e32 v64, v68, v66
	v_and_b32_e32 v65, 0xffff0000, v170
	v_fmac_f32_e32 v65, v69, v67
	v_bfe_u32 v66, v64, 16, 1
	v_add3_u32 v66, v64, v66, s51
	v_bfe_u32 v67, v65, 16, 1
	v_lshrrev_b32_e32 v66, 16, v66
	v_add3_u32 v67, v65, v67, s51
	v_and_or_b32 v66, v67, s48, v66
	v_lshl_add_u64 v[60:61], v[2:3], 0, v[60:61]
	global_store_dword v[60:61], v66, off
	s_waitcnt vmcnt(50)
	v_lshlrev_b32_e32 v60, 16, v171
	s_waitcnt vmcnt(49)
	v_fmac_f32_e32 v60, v64, v62
	v_and_b32_e32 v61, 0xffff0000, v171
	v_fmac_f32_e32 v61, v65, v63
	v_bfe_u32 v62, v60, 16, 1
	v_add3_u32 v62, v60, v62, s51
	v_bfe_u32 v63, v61, 16, 1
	v_lshrrev_b32_e32 v62, 16, v62
	v_add3_u32 v63, v61, v63, s51
	v_and_or_b32 v62, v63, s48, v62
	v_lshl_add_u64 v[56:57], v[2:3], 0, v[56:57]
	global_store_dword v[56:57], v62, off
	s_waitcnt vmcnt(49)
	v_lshlrev_b32_e32 v56, 16, v172
	s_waitcnt vmcnt(48)
	v_fmac_f32_e32 v56, v60, v58
	v_and_b32_e32 v57, 0xffff0000, v172
	v_fmac_f32_e32 v57, v61, v59
	v_bfe_u32 v58, v56, 16, 1
	v_add3_u32 v58, v56, v58, s51
	v_bfe_u32 v59, v57, 16, 1
	v_lshrrev_b32_e32 v58, 16, v58
	v_add3_u32 v59, v57, v59, s51
	v_and_or_b32 v58, v59, s48, v58
	v_lshl_add_u64 v[52:53], v[2:3], 0, v[52:53]
	global_store_dword v[52:53], v58, off
	s_waitcnt vmcnt(48)
	v_lshlrev_b32_e32 v52, 16, v173
	s_waitcnt vmcnt(47)
	v_fmac_f32_e32 v52, v56, v54
	v_and_b32_e32 v53, 0xffff0000, v173
	v_fmac_f32_e32 v53, v57, v55
	v_bfe_u32 v54, v52, 16, 1
	v_add3_u32 v54, v52, v54, s51
	v_bfe_u32 v55, v53, 16, 1
	v_lshrrev_b32_e32 v54, 16, v54
	v_add3_u32 v55, v53, v55, s51
	v_and_or_b32 v54, v55, s48, v54
	v_lshl_add_u64 v[48:49], v[2:3], 0, v[48:49]
	global_store_dword v[48:49], v54, off
	s_waitcnt vmcnt(47)
	v_lshlrev_b32_e32 v48, 16, v174
	s_waitcnt vmcnt(46)
	v_fmac_f32_e32 v48, v52, v50
	v_and_b32_e32 v49, 0xffff0000, v174
	v_fmac_f32_e32 v49, v53, v51
	v_bfe_u32 v50, v48, 16, 1
	v_add3_u32 v50, v48, v50, s51
	v_bfe_u32 v51, v49, 16, 1
	v_lshrrev_b32_e32 v50, 16, v50
	v_add3_u32 v51, v49, v51, s51
	v_and_or_b32 v50, v51, s48, v50
	v_lshl_add_u64 v[44:45], v[2:3], 0, v[44:45]
	global_store_dword v[44:45], v50, off
	s_waitcnt vmcnt(46)
	v_lshlrev_b32_e32 v44, 16, v175
	s_waitcnt vmcnt(45)
	v_fmac_f32_e32 v44, v48, v46
	v_and_b32_e32 v45, 0xffff0000, v175
	v_fmac_f32_e32 v45, v49, v47
	v_bfe_u32 v46, v44, 16, 1
	v_add3_u32 v46, v44, v46, s51
	v_bfe_u32 v47, v45, 16, 1
	v_lshrrev_b32_e32 v46, 16, v46
	v_add3_u32 v47, v45, v47, s51
	v_and_or_b32 v46, v47, s48, v46
	v_lshl_add_u64 v[40:41], v[2:3], 0, v[40:41]
	global_store_dword v[40:41], v46, off
	s_waitcnt vmcnt(45)
	v_lshlrev_b32_e32 v40, 16, v176
	s_waitcnt vmcnt(44)
	v_fmac_f32_e32 v40, v44, v42
	v_and_b32_e32 v41, 0xffff0000, v176
	v_fmac_f32_e32 v41, v45, v43
	v_bfe_u32 v42, v40, 16, 1
	v_add3_u32 v42, v40, v42, s51
	v_bfe_u32 v43, v41, 16, 1
	v_lshrrev_b32_e32 v42, 16, v42
	v_add3_u32 v43, v41, v43, s51
	v_and_or_b32 v42, v43, s48, v42
	v_lshl_add_u64 v[36:37], v[2:3], 0, v[36:37]
	global_store_dword v[36:37], v42, off
	s_waitcnt vmcnt(44)
	v_lshlrev_b32_e32 v36, 16, v177
	s_waitcnt vmcnt(43)
	v_fmac_f32_e32 v36, v40, v38
	v_and_b32_e32 v37, 0xffff0000, v177
	v_fmac_f32_e32 v37, v41, v39
	v_bfe_u32 v38, v36, 16, 1
	v_add3_u32 v38, v36, v38, s51
	v_bfe_u32 v39, v37, 16, 1
	v_lshrrev_b32_e32 v38, 16, v38
	v_add3_u32 v39, v37, v39, s51
	v_and_or_b32 v38, v39, s48, v38
	v_lshl_add_u64 v[32:33], v[2:3], 0, v[32:33]
	global_store_dword v[32:33], v38, off
	s_waitcnt vmcnt(43)
	v_lshlrev_b32_e32 v32, 16, v178
	s_waitcnt vmcnt(42)
	v_fmac_f32_e32 v32, v36, v34
	v_and_b32_e32 v33, 0xffff0000, v178
	v_fmac_f32_e32 v33, v37, v35
	v_bfe_u32 v34, v32, 16, 1
	v_add3_u32 v34, v32, v34, s51
	v_bfe_u32 v35, v33, 16, 1
	v_lshrrev_b32_e32 v34, 16, v34
	v_add3_u32 v35, v33, v35, s51
	v_and_or_b32 v34, v35, s48, v34
	v_lshl_add_u64 v[28:29], v[2:3], 0, v[28:29]
	global_store_dword v[28:29], v34, off
	s_waitcnt vmcnt(42)
	v_lshlrev_b32_e32 v28, 16, v179
	s_waitcnt vmcnt(41)
	v_fmac_f32_e32 v28, v32, v30
	v_and_b32_e32 v29, 0xffff0000, v179
	v_fmac_f32_e32 v29, v33, v31
	v_bfe_u32 v30, v28, 16, 1
	v_add3_u32 v30, v28, v30, s51
	v_bfe_u32 v31, v29, 16, 1
	v_lshrrev_b32_e32 v30, 16, v30
	v_add3_u32 v31, v29, v31, s51
	v_and_or_b32 v30, v31, s48, v30
	v_lshl_add_u64 v[24:25], v[2:3], 0, v[24:25]
	global_store_dword v[24:25], v30, off
	s_waitcnt vmcnt(41)
	v_lshlrev_b32_e32 v24, 16, v180
	s_waitcnt vmcnt(40)
	v_fmac_f32_e32 v24, v28, v26
	v_and_b32_e32 v25, 0xffff0000, v180
	v_fmac_f32_e32 v25, v29, v27
	v_bfe_u32 v26, v24, 16, 1
	v_add3_u32 v26, v24, v26, s51
	v_bfe_u32 v27, v25, 16, 1
	v_lshrrev_b32_e32 v26, 16, v26
	v_add3_u32 v27, v25, v27, s51
	v_and_or_b32 v26, v27, s48, v26
	v_lshl_add_u64 v[20:21], v[2:3], 0, v[20:21]
	global_store_dword v[20:21], v26, off
	s_waitcnt vmcnt(40)
	v_lshlrev_b32_e32 v20, 16, v181
	s_waitcnt vmcnt(39)
	v_fmac_f32_e32 v20, v24, v22
	v_and_b32_e32 v21, 0xffff0000, v181
	v_fmac_f32_e32 v21, v25, v23
	v_bfe_u32 v22, v20, 16, 1
	v_add3_u32 v22, v20, v22, s51
	v_bfe_u32 v23, v21, 16, 1
	v_lshrrev_b32_e32 v22, 16, v22
	v_add3_u32 v23, v21, v23, s51
	v_and_or_b32 v22, v23, s48, v22
	v_lshl_add_u64 v[16:17], v[2:3], 0, v[16:17]
	global_store_dword v[16:17], v22, off
	s_waitcnt vmcnt(39)
	v_lshlrev_b32_e32 v16, 16, v182
	s_waitcnt vmcnt(38)
	v_fmac_f32_e32 v16, v20, v18
	v_and_b32_e32 v17, 0xffff0000, v182
	v_fmac_f32_e32 v17, v21, v19
	v_bfe_u32 v18, v16, 16, 1
	v_add3_u32 v18, v16, v18, s51
	v_bfe_u32 v19, v17, 16, 1
	v_lshrrev_b32_e32 v18, 16, v18
	v_add3_u32 v19, v17, v19, s51
	v_and_or_b32 v18, v19, s48, v18
	v_lshl_add_u64 v[12:13], v[2:3], 0, v[12:13]
	global_store_dword v[12:13], v18, off
	s_waitcnt vmcnt(38)
	v_lshlrev_b32_e32 v12, 16, v183
	s_waitcnt vmcnt(37)
	v_fmac_f32_e32 v12, v16, v14
	v_and_b32_e32 v13, 0xffff0000, v183
	v_fmac_f32_e32 v13, v17, v15
	v_bfe_u32 v14, v12, 16, 1
	v_add3_u32 v14, v12, v14, s51
	v_bfe_u32 v15, v13, 16, 1
	v_lshrrev_b32_e32 v14, 16, v14
	v_add3_u32 v15, v13, v15, s51
	v_and_or_b32 v14, v15, s48, v14
	v_lshl_add_u64 v[8:9], v[2:3], 0, v[8:9]
	global_store_dword v[8:9], v14, off
	s_waitcnt vmcnt(37)
	v_lshlrev_b32_e32 v8, 16, v184
	s_waitcnt vmcnt(36)
	v_fmac_f32_e32 v8, v12, v10
	v_and_b32_e32 v9, 0xffff0000, v184
	v_fmac_f32_e32 v9, v13, v11
	v_bfe_u32 v10, v8, 16, 1
	v_add3_u32 v10, v8, v10, s51
	v_bfe_u32 v11, v9, 16, 1
	v_lshrrev_b32_e32 v10, 16, v10
	v_add3_u32 v11, v9, v11, s51
	v_and_or_b32 v10, v11, s48, v10
	v_lshl_add_u64 v[4:5], v[2:3], 0, v[4:5]
	global_store_dword v[4:5], v10, off
	s_waitcnt vmcnt(36)
	v_lshlrev_b32_e32 v4, 16, v185
	v_cndmask_b32_e64 v0, 4, 35, vcc
	s_waitcnt vmcnt(0)
	v_fmac_f32_e32 v4, v8, v6
	v_and_b32_e32 v5, 0xffff0000, v185
	v_mad_i32_i24 v0, v150, 36, v0
	v_fmac_f32_e32 v5, v9, v7
	v_bfe_u32 v6, v4, 16, 1
	v_ashrrev_i32_e32 v1, 31, v0
	v_add3_u32 v4, v4, v6, s51
	v_bfe_u32 v6, v5, 16, 1
	s_mov_b32 s12, 0x7ffff
	v_lshlrev_b64 v[0:1], 16, v[0:1]
	v_lshrrev_b32_e32 v4, 16, v4
	v_add3_u32 v5, v5, v6, s51
	v_cmp_lt_i32_e32 vcc, s12, v146
	v_and_or_b32 v4, v5, s48, v4
	v_lshl_add_u64 v[0:1], v[2:3], 0, v[0:1]
	v_add_u32_e32 v147, s13, v147
	s_or_b64 s[10:11], vcc, s[10:11]
	global_store_dword v[0:1], v4, off
	s_andn2_b64 exec, exec, s[10:11]
	s_cbranch_execnz .LBB0_993

.LBB0_1050:
	s_andn2_b64 vcc, exec, s[2:3]
	s_cbranch_vccnz .LBB0_1116
	v_readlane_b32 s2, v255, 35
	v_readlane_b32 s3, v255, 36
	s_and_b64 s[2:3], s[2:3], exec
	s_cselect_b32 s13, 4, 0
	s_xor_b32 s14, s13, 36
	s_lshl_b32 s15, s14, 4
	s_cmp_ge_i32 s12, s15
	s_cbranch_scc1 .LBB0_1062
	s_ashr_i32 s9, s8, 6
	s_add_u32 s4, s44, 0x1d518000
	s_addc_u32 s5, s45, 0
	s_add_u32 s6, s44, 0x22f18000
	v_readlane_b32 s2, v255, 37
	s_addc_u32 s7, s45, 0
	v_readlane_b32 s3, v255, 38
	s_lshl_b32 s76, s2, 8
	v_readlane_b32 s16, v254, 55
	s_lshl_b64 s[2:3], s[76:77], 2
	v_readlane_b32 s28, v255, 3
	v_readlane_b32 s29, v255, 4
	s_add_u32 s10, s28, s2
	s_addc_u32 s11, s29, s3
	s_lshl_b32 s2, s9, 5
	s_and_b32 s16, s9, 3
	s_and_b32 s9, s2, 0xffffff80
	v_lshrrev_b32_e32 v1, 2, v0
	v_and_b32_e32 v96, 48, v0
	v_and_b32_e32 v4, 63, v0
	v_and_b32_e32 v2, 15, v0
	v_and_or_b32 v44, v1, 12, s9
	v_lshl_add_u64 v[0:1], s[44:45], 0, v[96:97]
	s_mov_b64 s[2:3], 0x64dc8000
	v_lshl_add_u64 v[46:47], v[0:1], 0, s[2:3]
	s_ashr_i32 s2, s9, 31
	v_lshl_add_u32 v5, v2, 2, 0
	v_lshl_or_b32 v62, s16, 4, v2
	v_lshlrev_b32_e32 v2, 6, v2
	v_mov_b32_e32 v3, s2
	v_ashrrev_i32_e32 v45, 31, v44
	v_lshl_add_u32 v2, s9, 8, v2
	v_lshl_add_u64 v[48:49], v[44:45], 2, s[10:11]
	v_lshl_add_u64 v[0:1], v[0:1], 0, v[2:3]
	s_mov_b64 s[10:11], 0x27718000
	v_lshl_add_u64 v[50:51], v[0:1], 0, s[10:11]
	v_cvt_f32_ubyte0_e32 v0, s14
	v_rcp_iflag_f32_e32 v0, v0
	s_lshl_b32 s9, s16, 6
	v_add_u32_e32 v63, s9, v5
	s_sub_i32 s9, 0, s14
	v_mul_f32_e32 v0, 0x4f7ffffe, v0
	v_cvt_u32_f32_e32 v0, v0
	v_lshl_add_u32 v6, v4, 2, 0
	s_andn2_b32 s8, s8, 63
	v_cmp_gt_u32_e64 s[2:3], 16, v4
	v_readfirstlane_b32 s10, v0
	s_mul_i32 s9, s9, s10
	s_mul_hi_u32 s9, s10, s9
	s_add_i32 s16, s10, s9
	v_add_u32_e32 v64, s8, v6
	v_readlane_b32 s17, v254, 56
	v_readlane_b32 s18, v254, 57
	v_readlane_b32 s19, v254, 58
	v_readlane_b32 s20, v254, 59
	v_readlane_b32 s21, v254, 60
	v_readlane_b32 s22, v254, 61
	v_readlane_b32 s23, v254, 62
	v_readlane_b32 s24, v254, 63
	v_readlane_b32 s25, v255, 0
	v_readlane_b32 s26, v255, 1
	v_readlane_b32 s27, v255, 2
	v_readlane_b32 s30, v255, 5
	v_readlane_b32 s31, v255, 6
	s_branch .LBB0_1054

.LBB0_1059:
	s_lshl_b32 s9, s20, 4
	s_add_i32 s9, s18, s9
	s_mul_hi_i32 s21, s9, 36
	s_mul_i32 s9, s9, 36
	s_mul_i32 s76, s20, 0x2400
	s_add_u32 s20, s9, s17
	s_addc_u32 s21, s21, s19
	s_lshl_b64 s[20:21], s[20:21], 16
	v_lshl_add_u64 v[90:91], v[50:51], 0, s[20:21]
	v_lshl_add_u64 v[32:33], s[76:77], 0, v[52:53]
	v_lshlrev_b64 v[32:33], 10, v[32:33]
	v_lshl_add_u64 v[86:87], v[56:57], 0, v[32:33]
	s_mov_b32 s20, 1
	s_movk_i32 s76, 0x2000
	v_lshl_add_u64 v[92:93], v[90:91], 0, s[76:77]
	s_movk_i32 s76, 0x4000
	v_lshl_add_u64 v[94:95], v[90:91], 0, s[76:77]
	s_movk_i32 s76, 0x6000
	v_lshl_add_u64 v[98:99], v[90:91], 0, s[76:77]
	s_mov_b32 s76, 0x8000
	v_lshl_add_u64 v[100:101], v[90:91], 0, s[76:77]
	global_load_dwordx4 v[104:107], v[86:87], off
	global_load_dwordx4 v[120:123], v[90:91], off
	global_load_dwordx4 v[136:139], v[92:93], off offset:-4096
	global_load_dwordx4 v[152:155], v[92:93], off
	global_load_dwordx4 v[168:171], v[94:95], off offset:-4096
	global_load_dwordx4 v[184:187], v[94:95], off
	global_load_dwordx4 v[200:203], v[98:99], off offset:-4096
	global_load_dwordx4 v[218:221], v[98:99], off
	global_load_dwordx4 v[234:237], v[100:101], off offset:-4096
	global_load_dwordx4 v[108:111], v[86:87], off offset:64
	global_load_dwordx4 v[124:127], v[90:91], off offset:1024
	global_load_dwordx4 v[140:143], v[92:93], off offset:-3072
	global_load_dwordx4 v[156:159], v[92:93], off offset:1024
	global_load_dwordx4 v[172:175], v[94:95], off offset:-3072
	global_load_dwordx4 v[188:191], v[94:95], off offset:1024
	global_load_dwordx4 v[204:207], v[98:99], off offset:-3072
	global_load_dwordx4 v[222:225], v[98:99], off offset:1024
	global_load_dwordx4 v[238:241], v[100:101], off offset:-3072
	global_load_dwordx4 v[112:115], v[86:87], off offset:128
	global_load_dwordx4 v[128:131], v[90:91], off offset:2048
	global_load_dwordx4 v[144:147], v[92:93], off offset:-2048
	global_load_dwordx4 v[160:163], v[92:93], off offset:2048
	global_load_dwordx4 v[176:179], v[94:95], off offset:-2048
	global_load_dwordx4 v[192:195], v[94:95], off offset:2048
	global_load_dwordx4 v[208:211], v[98:99], off offset:-2048
	global_load_dwordx4 v[226:229], v[98:99], off offset:2048
	global_load_dwordx4 v[242:245], v[100:101], off offset:-2048
	global_load_dwordx4 v[116:119], v[86:87], off offset:192
	global_load_dwordx4 v[132:135], v[90:91], off offset:3072
	global_load_dwordx4 v[148:151], v[92:93], off offset:-1024
	global_load_dwordx4 v[164:167], v[92:93], off offset:3072
	global_load_dwordx4 v[180:183], v[94:95], off offset:-1024
	global_load_dwordx4 v[196:199], v[94:95], off offset:3072
	global_load_dwordx4 v[212:215], v[98:99], off offset:-1024
	global_load_dwordx4 v[230:233], v[98:99], off offset:3072
	global_load_dwordx4 v[246:249], v[100:101], off offset:-1024
	s_waitcnt vmcnt(34)
	v_mfma_f32_16x16x32_bf16 v[28:31], v[120:123], v[104:107], v[28:31]
	s_waitcnt vmcnt(33)
	v_mfma_f32_16x16x32_bf16 v[24:27], v[136:139], v[104:107], v[24:27]
	s_waitcnt vmcnt(32)
	v_mfma_f32_16x16x32_bf16 v[20:23], v[152:155], v[104:107], v[20:23]
	s_waitcnt vmcnt(31)
	v_mfma_f32_16x16x32_bf16 v[12:15], v[168:171], v[104:107], v[12:15]
	s_waitcnt vmcnt(30)
	v_mfma_f32_16x16x32_bf16 v[16:19], v[184:187], v[104:107], v[16:19]
	s_waitcnt vmcnt(29)
	v_mfma_f32_16x16x32_bf16 v[8:11], v[200:203], v[104:107], v[8:11]
	s_waitcnt vmcnt(28)
	v_mfma_f32_16x16x32_bf16 v[4:7], v[218:221], v[104:107], v[4:7]
	s_waitcnt vmcnt(27)
	v_mfma_f32_16x16x32_bf16 v[0:3], v[234:237], v[104:107], v[0:3]
	s_waitcnt vmcnt(25)
	v_mfma_f32_16x16x32_bf16 v[28:31], v[124:127], v[108:111], v[28:31]
	s_waitcnt vmcnt(24)
	v_mfma_f32_16x16x32_bf16 v[24:27], v[140:143], v[108:111], v[24:27]
	s_waitcnt vmcnt(23)
	v_mfma_f32_16x16x32_bf16 v[20:23], v[156:159], v[108:111], v[20:23]
	s_waitcnt vmcnt(22)
	v_mfma_f32_16x16x32_bf16 v[12:15], v[172:175], v[108:111], v[12:15]
	s_waitcnt vmcnt(21)
	v_mfma_f32_16x16x32_bf16 v[16:19], v[188:191], v[108:111], v[16:19]
	s_waitcnt vmcnt(20)
	v_mfma_f32_16x16x32_bf16 v[8:11], v[204:207], v[108:111], v[8:11]
	s_waitcnt vmcnt(19)
	v_mfma_f32_16x16x32_bf16 v[4:7], v[222:225], v[108:111], v[4:7]
	s_waitcnt vmcnt(18)
	v_mfma_f32_16x16x32_bf16 v[0:3], v[238:241], v[108:111], v[0:3]
	s_waitcnt vmcnt(16)
	v_mfma_f32_16x16x32_bf16 v[28:31], v[128:131], v[112:115], v[28:31]
	s_waitcnt vmcnt(15)
	v_mfma_f32_16x16x32_bf16 v[24:27], v[144:147], v[112:115], v[24:27]
	s_waitcnt vmcnt(14)
	v_mfma_f32_16x16x32_bf16 v[20:23], v[160:163], v[112:115], v[20:23]
	s_waitcnt vmcnt(13)
	v_mfma_f32_16x16x32_bf16 v[12:15], v[176:179], v[112:115], v[12:15]
	s_waitcnt vmcnt(12)
	v_mfma_f32_16x16x32_bf16 v[16:19], v[192:195], v[112:115], v[16:19]
	s_waitcnt vmcnt(11)
	v_mfma_f32_16x16x32_bf16 v[8:11], v[208:211], v[112:115], v[8:11]
	s_waitcnt vmcnt(10)
	v_mfma_f32_16x16x32_bf16 v[4:7], v[226:229], v[112:115], v[4:7]
	s_waitcnt vmcnt(9)
	v_mfma_f32_16x16x32_bf16 v[0:3], v[242:245], v[112:115], v[0:3]
	s_waitcnt vmcnt(7)
	v_mfma_f32_16x16x32_bf16 v[28:31], v[132:135], v[116:119], v[28:31]
	s_waitcnt vmcnt(6)
	v_mfma_f32_16x16x32_bf16 v[24:27], v[148:151], v[116:119], v[24:27]
	s_waitcnt vmcnt(5)
	v_mfma_f32_16x16x32_bf16 v[20:23], v[164:167], v[116:119], v[20:23]
	s_waitcnt vmcnt(4)
	v_mfma_f32_16x16x32_bf16 v[12:15], v[180:183], v[116:119], v[12:15]
	s_waitcnt vmcnt(3)
	v_mfma_f32_16x16x32_bf16 v[16:19], v[196:199], v[116:119], v[16:19]
	s_waitcnt vmcnt(2)
	v_mfma_f32_16x16x32_bf16 v[8:11], v[212:215], v[116:119], v[8:11]
	s_waitcnt vmcnt(1)
	v_mfma_f32_16x16x32_bf16 v[4:7], v[230:233], v[116:119], v[4:7]
	s_waitcnt vmcnt(0)
	v_mfma_f32_16x16x32_bf16 v[0:3], v[246:249], v[116:119], v[0:3]
	s_nop 1
	v_cndmask_b32_e64 v40, 0, 1, s[10:11]
	v_cmp_ne_u32_e32 vcc, 1, v40
	s_mov_b64 s[10:11], 0
	s_cbranch_vccz .LBB0_1059
	v_mul_f32_e32 v32, v29, v29
	v_mul_f32_e32 v33, v25, v25
	v_fmac_f32_e32 v32, v28, v28
	v_fmac_f32_e32 v33, v24, v24
	v_fmac_f32_e32 v32, v30, v30
	v_fmac_f32_e32 v33, v26, v26
	v_fmac_f32_e32 v32, v31, v31
	v_fmac_f32_e32 v33, v27, v27
	v_add_f32_e32 v32, v32, v33
	v_mul_f32_e32 v33, v21, v21
	v_fmac_f32_e32 v33, v20, v20
	v_fmac_f32_e32 v33, v22, v22
	v_fmac_f32_e32 v33, v23, v23
	v_add_f32_e32 v32, v32, v33
	v_mul_f32_e32 v33, v13, v13
	v_fmac_f32_e32 v33, v12, v12
	v_fmac_f32_e32 v33, v14, v14
	v_fmac_f32_e32 v33, v15, v15
	v_add_f32_e32 v32, v32, v33
	v_mul_f32_e32 v33, v17, v17
	v_fmac_f32_e32 v33, v16, v16
	v_fmac_f32_e32 v33, v18, v18
	v_fmac_f32_e32 v33, v19, v19
	v_add_f32_e32 v32, v32, v33
	v_mul_f32_e32 v33, v9, v9
	v_fmac_f32_e32 v33, v8, v8
	v_fmac_f32_e32 v33, v10, v10
	v_fmac_f32_e32 v33, v11, v11
	v_add_f32_e32 v32, v32, v33
	v_mul_f32_e32 v33, v5, v5
	v_fmac_f32_e32 v33, v4, v4
	v_fmac_f32_e32 v33, v6, v6
	v_fmac_f32_e32 v33, v7, v7
	v_add_f32_e32 v32, v32, v33
	v_mul_f32_e32 v33, v1, v1
	v_fmac_f32_e32 v33, v0, v0
	v_fmac_f32_e32 v33, v2, v2
	v_fmac_f32_e32 v33, v3, v3
	v_add_f32_e32 v32, v32, v33
	ds_swizzle_b32 v33, v32 offset:swizzle(SWAP,16)
	s_waitcnt lgkmcnt(0)
	s_barrier
	v_add_f32_e32 v32, v32, v33
	v_mov_b32_e32 v33, v32
	s_nop 1
	v_permlane32_swap_b32_e32 v32, v33
	s_and_saveexec_b64 s[10:11], s[2:3]
	s_cbranch_execz .LBB0_1053
	v_add_f32_e32 v32, v32, v33
	ds_write_b32 v64, v32
	s_branch .LBB0_1053
